# lean stack: only the edits that measured as gains (router pass-2/pass-1 load batching, MoE-down epilogue load hoist, mix_unit weight-load hoist, HGRN A-block LDS pipelining, out-proj epilogue drain re
# baseline (speedup 1.0000x reference)
.LBB0_499:
	s_or_b64 exec, exec, s[22:23]
	v_pk_add_f32 v[64:65], v[162:163], v[100:101]
	s_add_i32 s26, s26, 2
	v_pk_add_f32 v[64:65], v[170:171], v[64:65]
	s_cmp_lg_u32 s19, s27
	v_pk_add_f32 v[64:65], v[102:103], v[64:65]
	s_waitcnt vmcnt(0)
	ds_write_b128 v62, v[94:97] offset:35840
	v_pk_add_f32 v[64:65], v[168:169], v[64:65]
	s_waitcnt lgkmcnt(0)
	v_pk_add_f32 v[64:65], v[104:105], v[64:65]
	s_barrier
	v_pk_add_f32 v[64:65], v[166:167], v[64:65]
	s_nop 0
	v_pk_add_f32 v[64:65], v[106:107], v[64:65]
	s_nop 0
	v_pk_add_f32 v[64:65], v[172:173], v[64:65]
	s_nop 0
	v_pk_add_f32 v[64:65], v[112:113], v[64:65]
	s_nop 0
	v_pk_add_f32 v[64:65], v[178:179], v[64:65]
	s_nop 0
	v_pk_add_f32 v[64:65], v[110:111], v[64:65]
	s_nop 0
	v_pk_add_f32 v[64:65], v[176:177], v[64:65]
	s_nop 0
	v_pk_add_f32 v[64:65], v[108:109], v[64:65]
	s_nop 0
	v_pk_add_f32 v[64:65], v[174:175], v[64:65]
	s_nop 0
	v_pk_add_f32 v[64:65], v[164:165], v[64:65]
	s_nop 0
	v_pk_add_f32 v[64:65], v[180:181], v[64:65]
	s_nop 0
	v_pk_add_f32 v[64:65], v[64:65], v[66:67]
	s_nop 0
	v_pk_add_f32 v[64:65], v[80:81], v[64:65]
	s_nop 0
	v_pk_add_f32 v[64:65], v[68:69], v[64:65]
	s_nop 0
	v_pk_add_f32 v[52:53], v[52:53], v[64:65]
	s_nop 0
	v_pk_add_f32 v[52:53], v[70:71], v[52:53]
	s_nop 0
	v_pk_add_f32 v[50:51], v[50:51], v[52:53]
	s_nop 0
	v_pk_add_f32 v[50:51], v[72:73], v[50:51]
	s_nop 0
	v_pk_add_f32 v[50:51], v[54:55], v[50:51]
	s_nop 0
	v_pk_add_f32 v[50:51], v[182:183], v[50:51]
	s_nop 0
	v_pk_add_f32 v[50:51], v[184:185], v[50:51]
	s_nop 0
	v_pk_add_f32 v[50:51], v[76:77], v[50:51]
	s_nop 0
	v_pk_add_f32 v[50:51], v[58:59], v[50:51]
	s_nop 0
	v_pk_add_f32 v[50:51], v[74:75], v[50:51]
	s_nop 0
	v_pk_add_f32 v[50:51], v[56:57], v[50:51]
	s_nop 0
	v_pk_add_f32 v[50:51], v[78:79], v[50:51]
	s_nop 0
	v_pk_add_f32 v[162:163], v[60:61], v[50:51]
	s_cbranch_scc0 .LBB0_509

.LBB0_504:
	s_or_b64 exec, exec, s[22:23]
	s_and_b32 s21, s26, 2
	s_mulk_i32 s21, 0x5800
	v_add_u32_e32 v96, s21, v195
	v_lshlrev_b32_e32 v97, 1, v160
	v_add_u32_e32 v112, v96, v97
	ds_read_b128 v[50:53], v112
	ds_read_b128 v[100:103], v112 offset:32
	ds_read_b128 v[104:107], v112 offset:6656
	ds_read_b128 v[108:111], v112 offset:6688
	v_add_u32_e32 v96, v96, v197
	s_waitcnt lgkmcnt(3)
	v_mfma_f32_32x32x16_bf16 v[66:81], v[50:53], v[144:147], v[2:17]
	v_lshl_add_u32 v206, v150, 1, v96
	v_add_u32_e32 v175, 0x3000, v206
	v_add_u32_e32 v182, 0x4000, v206
	v_add3_u32 v207, v96, v196, v97
	v_add_u32_e32 v211, 0x9800, v206
	v_add_u32_e32 v210, 0x8800, v206
	s_add_i32 s27, s27, 1
	s_waitcnt lgkmcnt(2)
	v_mfma_f32_32x32x16_bf16 v[66:81], v[100:103], v[140:143], v[66:81]
	s_bitcmp1_b32 s27, 0
	s_cselect_b32 s21, 0xb000, 0
	s_add_i32 s21, s21, 0
	s_waitcnt lgkmcnt(1)
	v_mfma_f32_32x32x16_bf16 v[50:65], v[104:107], v[144:147], v[2:17]
	ds_read_b128 v[100:103], v112 offset:64
	ds_read_b128 v[104:107], v112 offset:96
	s_waitcnt lgkmcnt(1)
	v_mfma_f32_32x32x16_bf16 v[66:81], v[100:103], v[136:139], v[66:81]
	v_mfma_f32_32x32x16_bf16 v[50:65], v[108:111], v[140:143], v[50:65]
	ds_read_b128 v[100:103], v112 offset:6720
	ds_read_b128 v[108:111], v112 offset:6752
	s_waitcnt lgkmcnt(2)
	v_mfma_f32_32x32x16_bf16 v[66:81], v[104:107], v[132:135], v[66:81]
	s_waitcnt lgkmcnt(1)
	v_mfma_f32_32x32x16_bf16 v[50:65], v[100:103], v[136:139], v[50:65]
	ds_read_b128 v[100:103], v112 offset:128
	ds_read_b128 v[104:107], v112 offset:160
	s_waitcnt lgkmcnt(1)
	v_mfma_f32_32x32x16_bf16 v[66:81], v[100:103], v[128:131], v[66:81]
	v_mfma_f32_32x32x16_bf16 v[50:65], v[108:111], v[132:135], v[50:65]
	ds_read_b128 v[100:103], v112 offset:6784
	ds_read_b128 v[108:111], v112 offset:6816
	s_waitcnt lgkmcnt(2)
	v_mfma_f32_32x32x16_bf16 v[66:81], v[104:107], v[124:127], v[66:81]
	s_waitcnt lgkmcnt(1)
	v_mfma_f32_32x32x16_bf16 v[50:65], v[100:103], v[128:131], v[50:65]
	s_nop 9
	v_exp_f32_e32 v100, v66
	v_exp_f32_e32 v101, v67
	v_exp_f32_e32 v102, v68
	v_exp_f32_e32 v103, v69
	ds_read2_b64 v[66:69], v175 offset0:128 offset1:130
	v_exp_f32_e32 v104, v70
	v_exp_f32_e32 v105, v71
	v_exp_f32_e32 v106, v72
	v_exp_f32_e32 v107, v73
	v_cvt_pk_bf16_f32 v70, v100, v101
	v_cvt_pk_bf16_f32 v71, v102, v103
	v_cvt_pk_bf16_f32 v72, v104, v105
	v_cvt_pk_bf16_f32 v73, v106, v107
	s_waitcnt lgkmcnt(1)
	v_mfma_f32_32x32x16_bf16 v[50:65], v[108:111], v[124:127], v[50:65]
	v_exp_f32_e32 v112, v74
	v_exp_f32_e32 v113, v75
	v_exp_f32_e32 v110, v76
	v_exp_f32_e32 v111, v77
	ds_read2_b64 v[74:77], v175 offset0:132 offset1:134
	v_exp_f32_e32 v108, v78
	v_exp_f32_e32 v109, v79
	s_waitcnt lgkmcnt(1)
	v_mfma_f32_32x32x16_bf16 v[18:33], v[66:69], v[70:73], v[18:33]
	ds_read2_b64 v[66:69], v182 offset0:192 offset1:194
	v_exp_f32_e32 v164, v80
	v_exp_f32_e32 v165, v81
	v_exp_f32_e32 v170, v50
	v_exp_f32_e32 v171, v51
	v_exp_f32_e32 v168, v52
	v_exp_f32_e32 v169, v53
	s_waitcnt lgkmcnt(0)
	v_mfma_f32_32x32x16_bf16 v[34:49], v[66:69], v[70:73], v[34:49]
	v_cvt_pk_bf16_f32 v66, v112, v113
	v_cvt_pk_bf16_f32 v67, v110, v111
	v_cvt_pk_bf16_f32 v68, v108, v109
	v_cvt_pk_bf16_f32 v69, v164, v165
	ds_read2_b64 v[50:53], v175 offset0:136 offset1:138
	ds_read2_b64 v[70:73], v182 offset0:196 offset1:198
	v_exp_f32_e32 v166, v54
	v_mfma_f32_32x32x16_bf16 v[18:33], v[74:77], v[66:69], v[18:33]
	v_exp_f32_e32 v167, v55
	v_exp_f32_e32 v172, v56
	v_exp_f32_e32 v173, v57
	v_cvt_pk_bf16_f32 v54, v170, v171
	v_cvt_pk_bf16_f32 v55, v168, v169
	v_cvt_pk_bf16_f32 v56, v166, v167
	v_cvt_pk_bf16_f32 v57, v172, v173
	s_waitcnt lgkmcnt(0)
	v_mfma_f32_32x32x16_bf16 v[34:49], v[70:73], v[66:69], v[34:49]
	v_exp_f32_e32 v178, v58
	v_exp_f32_e32 v179, v59
	v_exp_f32_e32 v176, v60
	v_exp_f32_e32 v177, v61
	ds_read2_b64 v[58:61], v175 offset0:140 offset1:142
	v_exp_f32_e32 v174, v62
	v_exp_f32_e32 v175, v63
	v_mfma_f32_32x32x16_bf16 v[18:33], v[50:53], v[54:57], v[18:33]
	ds_read2_b64 v[50:53], v182 offset0:200 offset1:202
	v_exp_f32_e32 v180, v64
	v_exp_f32_e32 v181, v65
	s_waitcnt lgkmcnt(0)
	v_mfma_f32_32x32x16_bf16 v[34:49], v[50:53], v[54:57], v[34:49]
	ds_read2_b64 v[54:57], v182 offset0:204 offset1:206
	v_cvt_pk_bf16_f32 v50, v178, v179
	v_cvt_pk_bf16_f32 v51, v176, v177
	v_cvt_pk_bf16_f32 v52, v174, v175
	v_cvt_pk_bf16_f32 v53, v180, v181
	s_nop 1
	v_mfma_f32_32x32x16_bf16 v[18:33], v[58:61], v[50:53], v[18:33]
	s_waitcnt lgkmcnt(0)
	v_mfma_f32_32x32x16_bf16 v[34:49], v[54:57], v[50:53], v[34:49]
	ds_read_b128 v[50:53], v207 offset:22528
	ds_read_b128 v[182:185], v207 offset:22560
	ds_read_b128 v[198:201], v207 offset:29184
	ds_read_b128 v[202:205], v207 offset:29216
	s_waitcnt lgkmcnt(3)
	v_mfma_f32_32x32x16_bf16 v[66:81], v[50:53], v[144:147], v[2:17]
	s_waitcnt lgkmcnt(1)
	v_mfma_f32_32x32x16_bf16 v[50:65], v[198:201], v[144:147], v[2:17]
	v_mfma_f32_32x32x16_bf16 v[66:81], v[182:185], v[140:143], v[66:81]
	ds_read_b128 v[182:185], v207 offset:22592
	ds_read_b128 v[198:201], v207 offset:22624
	s_waitcnt lgkmcnt(2)
	v_mfma_f32_32x32x16_bf16 v[50:65], v[202:205], v[140:143], v[50:65]
	s_waitcnt lgkmcnt(1)
	v_mfma_f32_32x32x16_bf16 v[66:81], v[182:185], v[136:139], v[66:81]
	ds_read_b128 v[182:185], v207 offset:29248
	ds_read_b128 v[202:205], v207 offset:29280
	s_waitcnt lgkmcnt(1)
	v_mfma_f32_32x32x16_bf16 v[50:65], v[182:185], v[136:139], v[50:65]
	v_mfma_f32_32x32x16_bf16 v[66:81], v[198:201], v[132:135], v[66:81]
	ds_read_b128 v[182:185], v207 offset:22656
	ds_read_b128 v[198:201], v207 offset:22688
	global_load_dwordx4 v[94:97], v[94:95], off offset:128
	s_waitcnt lgkmcnt(1)
	v_mfma_f32_32x32x16_bf16 v[66:81], v[182:185], v[128:131], v[66:81]
	ds_read_b128 v[182:185], v207 offset:29312
	v_mfma_f32_32x32x16_bf16 v[50:65], v[202:205], v[132:135], v[50:65]
	ds_read2_b64 v[202:205], v211 offset0:192 offset1:194
	s_waitcnt lgkmcnt(2)
	v_mfma_f32_32x32x16_bf16 v[66:81], v[198:201], v[124:127], v[66:81]
	ds_read_b128 v[198:201], v207 offset:29344
	ds_read2_b64 v[206:209], v210 offset0:132 offset1:134
	s_waitcnt lgkmcnt(3)
	v_mfma_f32_32x32x16_bf16 v[50:65], v[182:185], v[128:131], v[50:65]
	ds_read2_b64 v[182:185], v210 offset0:128 offset1:130
	s_nop 6
	v_exp_f32_e32 v66, v66
	v_exp_f32_e32 v67, v67
	v_exp_f32_e32 v68, v68
	v_exp_f32_e32 v69, v69
	v_exp_f32_e32 v70, v70
	v_exp_f32_e32 v71, v71
	v_exp_f32_e32 v72, v72
	v_exp_f32_e32 v73, v73
	s_waitcnt lgkmcnt(2)
	v_mfma_f32_32x32x16_bf16 v[50:65], v[198:201], v[124:127], v[50:65]
	v_cvt_pk_bf16_f32 v198, v66, v67
	v_cvt_pk_bf16_f32 v199, v68, v69
	v_cvt_pk_bf16_f32 v200, v70, v71
	v_cvt_pk_bf16_f32 v201, v72, v73
	v_exp_f32_e32 v76, v76
	v_exp_f32_e32 v77, v77
	s_nop 5
	v_exp_f32_e32 v52, v52
	v_mfma_f32_32x32x16_bf16 v[34:49], v[202:205], v[198:201], v[34:49]
	ds_read2_b64 v[202:205], v211 offset0:196 offset1:198
	v_exp_f32_e32 v53, v53
	s_waitcnt lgkmcnt(1)
	v_mfma_f32_32x32x16_bf16 v[18:33], v[182:185], v[198:201], v[18:33]
	v_exp_f32_e32 v182, v74
	v_exp_f32_e32 v183, v75
	v_exp_f32_e32 v74, v78
	v_exp_f32_e32 v75, v79
	v_exp_f32_e32 v78, v80
	v_exp_f32_e32 v79, v81
	v_cvt_pk_bf16_f32 v198, v182, v183
	v_cvt_pk_bf16_f32 v199, v76, v77
	v_cvt_pk_bf16_f32 v200, v74, v75
	v_cvt_pk_bf16_f32 v201, v78, v79
	v_exp_f32_e32 v80, v50
	v_exp_f32_e32 v81, v51
	v_mfma_f32_32x32x16_bf16 v[18:33], v[206:209], v[198:201], v[18:33]
	ds_read2_b64 v[206:209], v210 offset0:136 offset1:138
	v_exp_f32_e32 v50, v54
	v_exp_f32_e32 v51, v55
	v_exp_f32_e32 v54, v56
	v_exp_f32_e32 v55, v57
	v_exp_f32_e32 v184, v58
	v_exp_f32_e32 v185, v59
	s_waitcnt lgkmcnt(1)
	v_mfma_f32_32x32x16_bf16 v[34:49], v[202:205], v[198:201], v[34:49]
	ds_read2_b64 v[202:205], v211 offset0:200 offset1:202
	v_cvt_pk_bf16_f32 v198, v80, v81
	v_cvt_pk_bf16_f32 v199, v52, v53
	v_cvt_pk_bf16_f32 v200, v50, v51
	v_cvt_pk_bf16_f32 v201, v54, v55
	v_exp_f32_e32 v58, v60
	v_exp_f32_e32 v59, v61
	s_waitcnt lgkmcnt(1)
	v_mfma_f32_32x32x16_bf16 v[18:33], v[206:209], v[198:201], v[18:33]
	ds_read2_b64 v[206:209], v210 offset0:140 offset1:142
	v_exp_f32_e32 v56, v62
	v_exp_f32_e32 v57, v63
	v_exp_f32_e32 v60, v64
	v_exp_f32_e32 v61, v65
	v_add_u32_e32 v63, s21, v188
	v_add_u32_e32 v62, s21, v189
	s_waitcnt lgkmcnt(1)
	v_mfma_f32_32x32x16_bf16 v[34:49], v[202:205], v[198:201], v[34:49]
	ds_read2_b64 v[202:205], v211 offset0:204 offset1:206
	v_cvt_pk_bf16_f32 v198, v184, v185
	v_cvt_pk_bf16_f32 v199, v58, v59
	v_cvt_pk_bf16_f32 v200, v56, v57
	v_cvt_pk_bf16_f32 v201, v60, v61
	s_waitcnt vmcnt(3)
	ds_write_b128 v63, v[90:93]
	s_waitcnt lgkmcnt(2)
	v_mfma_f32_32x32x16_bf16 v[18:33], v[206:209], v[198:201], v[18:33]
	s_waitcnt lgkmcnt(1)
	v_mfma_f32_32x32x16_bf16 v[34:49], v[202:205], v[198:201], v[34:49]
	s_and_saveexec_b64 s[22:23], s[0:1]
	s_xor_b64 s[22:23], exec, s[22:23]
	s_cbranch_execz .LBB0_506
	s_waitcnt vmcnt(2)
	ds_write_b128 v62, v[82:85] offset:13312
	s_waitcnt vmcnt(1)
	ds_write_b128 v63, v[86:89] offset:22528

.LBB0_549:
	s_or_b64 exec, exec, s[16:17]
	v_pk_add_f32 v[64:65], v[162:163], v[100:101]
	s_add_i32 s22, s22, 2
	v_pk_add_f32 v[64:65], v[170:171], v[64:65]
	s_cmp_lg_u32 s3, s23
	v_pk_add_f32 v[64:65], v[102:103], v[64:65]
	s_waitcnt vmcnt(0)
	ds_write_b128 v62, v[94:97] offset:35840
	v_pk_add_f32 v[64:65], v[168:169], v[64:65]
	s_waitcnt lgkmcnt(0)
	v_pk_add_f32 v[64:65], v[104:105], v[64:65]
	s_barrier
	v_pk_add_f32 v[64:65], v[166:167], v[64:65]
	s_nop 0
	v_pk_add_f32 v[64:65], v[106:107], v[64:65]
	s_nop 0
	v_pk_add_f32 v[64:65], v[172:173], v[64:65]
	s_nop 0
	v_pk_add_f32 v[64:65], v[112:113], v[64:65]
	s_nop 0
	v_pk_add_f32 v[64:65], v[178:179], v[64:65]
	s_nop 0
	v_pk_add_f32 v[64:65], v[110:111], v[64:65]
	s_nop 0
	v_pk_add_f32 v[64:65], v[176:177], v[64:65]
	s_nop 0
	v_pk_add_f32 v[64:65], v[108:109], v[64:65]
	s_nop 0
	v_pk_add_f32 v[64:65], v[174:175], v[64:65]
	s_nop 0
	v_pk_add_f32 v[64:65], v[164:165], v[64:65]
	s_nop 0
	v_pk_add_f32 v[64:65], v[180:181], v[64:65]
	s_nop 0
	v_pk_add_f32 v[64:65], v[64:65], v[66:67]
	s_nop 0
	v_pk_add_f32 v[64:65], v[80:81], v[64:65]
	s_nop 0
	v_pk_add_f32 v[64:65], v[68:69], v[64:65]
	s_nop 0
	v_pk_add_f32 v[52:53], v[52:53], v[64:65]
	s_nop 0
	v_pk_add_f32 v[52:53], v[70:71], v[52:53]
	s_nop 0
	v_pk_add_f32 v[50:51], v[50:51], v[52:53]
	s_nop 0
	v_pk_add_f32 v[50:51], v[72:73], v[50:51]
	s_nop 0
	v_pk_add_f32 v[50:51], v[54:55], v[50:51]
	s_nop 0
	v_pk_add_f32 v[50:51], v[182:183], v[50:51]
	s_nop 0
	v_pk_add_f32 v[50:51], v[184:185], v[50:51]
	s_nop 0
	v_pk_add_f32 v[50:51], v[76:77], v[50:51]
	s_nop 0
	v_pk_add_f32 v[50:51], v[58:59], v[50:51]
	s_nop 0
	v_pk_add_f32 v[50:51], v[74:75], v[50:51]
	s_nop 0
	v_pk_add_f32 v[50:51], v[56:57], v[50:51]
	s_nop 0
	v_pk_add_f32 v[50:51], v[78:79], v[50:51]
	s_nop 0
	v_pk_add_f32 v[162:163], v[60:61], v[50:51]
	s_cbranch_scc0 .LBB0_559

.LBB0_554:
	s_or_b64 exec, exec, s[16:17]
	s_and_b32 s15, s22, 2
	s_mulk_i32 s15, 0x5800
	v_add_u32_e32 v96, s15, v195
	v_lshlrev_b32_e32 v97, 1, v160
	v_add_u32_e32 v112, v96, v97
	ds_read_b128 v[50:53], v112
	ds_read_b128 v[100:103], v112 offset:32
	ds_read_b128 v[104:107], v112 offset:6656
	ds_read_b128 v[108:111], v112 offset:6688
	v_add_u32_e32 v96, v96, v197
	s_waitcnt lgkmcnt(3)
	v_mfma_f32_32x32x16_bf16 v[66:81], v[50:53], v[144:147], v[2:17]
	v_lshl_add_u32 v206, v150, 1, v96
	v_add_u32_e32 v175, 0x3000, v206
	v_add_u32_e32 v182, 0x4000, v206
	v_add3_u32 v207, v96, v196, v97
	v_add_u32_e32 v211, 0x9800, v206
	v_add_u32_e32 v210, 0x8800, v206
	s_add_i32 s23, s23, 1
	s_waitcnt lgkmcnt(2)
	v_mfma_f32_32x32x16_bf16 v[66:81], v[100:103], v[140:143], v[66:81]
	s_bitcmp1_b32 s23, 0
	s_cselect_b32 s15, 0xb000, 0
	s_add_i32 s15, s15, 0
	s_waitcnt lgkmcnt(1)
	v_mfma_f32_32x32x16_bf16 v[50:65], v[104:107], v[144:147], v[2:17]
	ds_read_b128 v[100:103], v112 offset:64
	ds_read_b128 v[104:107], v112 offset:96
	s_waitcnt lgkmcnt(1)
	v_mfma_f32_32x32x16_bf16 v[66:81], v[100:103], v[136:139], v[66:81]
	v_mfma_f32_32x32x16_bf16 v[50:65], v[108:111], v[140:143], v[50:65]
	ds_read_b128 v[100:103], v112 offset:6720
	ds_read_b128 v[108:111], v112 offset:6752
	s_waitcnt lgkmcnt(2)
	v_mfma_f32_32x32x16_bf16 v[66:81], v[104:107], v[132:135], v[66:81]
	s_waitcnt lgkmcnt(1)
	v_mfma_f32_32x32x16_bf16 v[50:65], v[100:103], v[136:139], v[50:65]
	ds_read_b128 v[100:103], v112 offset:128
	ds_read_b128 v[104:107], v112 offset:160
	s_waitcnt lgkmcnt(1)
	v_mfma_f32_32x32x16_bf16 v[66:81], v[100:103], v[128:131], v[66:81]
	v_mfma_f32_32x32x16_bf16 v[50:65], v[108:111], v[132:135], v[50:65]
	ds_read_b128 v[100:103], v112 offset:6784
	ds_read_b128 v[108:111], v112 offset:6816
	s_waitcnt lgkmcnt(2)
	v_mfma_f32_32x32x16_bf16 v[66:81], v[104:107], v[124:127], v[66:81]
	s_waitcnt lgkmcnt(1)
	v_mfma_f32_32x32x16_bf16 v[50:65], v[100:103], v[128:131], v[50:65]
	s_nop 9
	v_exp_f32_e32 v100, v66
	v_exp_f32_e32 v101, v67
	v_exp_f32_e32 v102, v68
	v_exp_f32_e32 v103, v69
	ds_read2_b64 v[66:69], v175 offset0:128 offset1:130
	v_exp_f32_e32 v104, v70
	v_exp_f32_e32 v105, v71
	v_exp_f32_e32 v106, v72
	v_exp_f32_e32 v107, v73
	v_cvt_pk_bf16_f32 v70, v100, v101
	v_cvt_pk_bf16_f32 v71, v102, v103
	v_cvt_pk_bf16_f32 v72, v104, v105
	v_cvt_pk_bf16_f32 v73, v106, v107
	s_waitcnt lgkmcnt(1)
	v_mfma_f32_32x32x16_bf16 v[50:65], v[108:111], v[124:127], v[50:65]
	v_exp_f32_e32 v112, v74
	v_exp_f32_e32 v113, v75
	v_exp_f32_e32 v110, v76
	v_exp_f32_e32 v111, v77
	ds_read2_b64 v[74:77], v175 offset0:132 offset1:134
	v_exp_f32_e32 v108, v78
	v_exp_f32_e32 v109, v79
	s_waitcnt lgkmcnt(1)
	v_mfma_f32_32x32x16_bf16 v[18:33], v[66:69], v[70:73], v[18:33]
	ds_read2_b64 v[66:69], v182 offset0:192 offset1:194
	v_exp_f32_e32 v164, v80
	v_exp_f32_e32 v165, v81
	v_exp_f32_e32 v170, v50
	v_exp_f32_e32 v171, v51
	v_exp_f32_e32 v168, v52
	v_exp_f32_e32 v169, v53
	s_waitcnt lgkmcnt(0)
	v_mfma_f32_32x32x16_bf16 v[34:49], v[66:69], v[70:73], v[34:49]
	v_cvt_pk_bf16_f32 v66, v112, v113
	v_cvt_pk_bf16_f32 v67, v110, v111
	v_cvt_pk_bf16_f32 v68, v108, v109
	v_cvt_pk_bf16_f32 v69, v164, v165
	ds_read2_b64 v[50:53], v175 offset0:136 offset1:138
	ds_read2_b64 v[70:73], v182 offset0:196 offset1:198
	v_exp_f32_e32 v166, v54
	v_mfma_f32_32x32x16_bf16 v[18:33], v[74:77], v[66:69], v[18:33]
	v_exp_f32_e32 v167, v55
	v_exp_f32_e32 v172, v56
	v_exp_f32_e32 v173, v57
	v_cvt_pk_bf16_f32 v54, v170, v171
	v_cvt_pk_bf16_f32 v55, v168, v169
	v_cvt_pk_bf16_f32 v56, v166, v167
	v_cvt_pk_bf16_f32 v57, v172, v173
	s_waitcnt lgkmcnt(0)
	v_mfma_f32_32x32x16_bf16 v[34:49], v[70:73], v[66:69], v[34:49]
	v_exp_f32_e32 v178, v58
	v_exp_f32_e32 v179, v59
	v_exp_f32_e32 v176, v60
	v_exp_f32_e32 v177, v61
	ds_read2_b64 v[58:61], v175 offset0:140 offset1:142
	v_exp_f32_e32 v174, v62
	v_exp_f32_e32 v175, v63
	v_mfma_f32_32x32x16_bf16 v[18:33], v[50:53], v[54:57], v[18:33]
	ds_read2_b64 v[50:53], v182 offset0:200 offset1:202
	v_exp_f32_e32 v180, v64
	v_exp_f32_e32 v181, v65
	s_waitcnt lgkmcnt(0)
	v_mfma_f32_32x32x16_bf16 v[34:49], v[50:53], v[54:57], v[34:49]
	ds_read2_b64 v[54:57], v182 offset0:204 offset1:206
	v_cvt_pk_bf16_f32 v50, v178, v179
	v_cvt_pk_bf16_f32 v51, v176, v177
	v_cvt_pk_bf16_f32 v52, v174, v175
	v_cvt_pk_bf16_f32 v53, v180, v181
	s_nop 1
	v_mfma_f32_32x32x16_bf16 v[18:33], v[58:61], v[50:53], v[18:33]
	s_waitcnt lgkmcnt(0)
	v_mfma_f32_32x32x16_bf16 v[34:49], v[54:57], v[50:53], v[34:49]
	ds_read_b128 v[50:53], v207 offset:22528
	ds_read_b128 v[182:185], v207 offset:22560
	ds_read_b128 v[198:201], v207 offset:29184
	ds_read_b128 v[202:205], v207 offset:29216
	s_waitcnt lgkmcnt(3)
	v_mfma_f32_32x32x16_bf16 v[66:81], v[50:53], v[144:147], v[2:17]
	s_waitcnt lgkmcnt(1)
	v_mfma_f32_32x32x16_bf16 v[50:65], v[198:201], v[144:147], v[2:17]
	v_mfma_f32_32x32x16_bf16 v[66:81], v[182:185], v[140:143], v[66:81]
	ds_read_b128 v[182:185], v207 offset:22592
	ds_read_b128 v[198:201], v207 offset:22624
	s_waitcnt lgkmcnt(2)
	v_mfma_f32_32x32x16_bf16 v[50:65], v[202:205], v[140:143], v[50:65]
	s_waitcnt lgkmcnt(1)
	v_mfma_f32_32x32x16_bf16 v[66:81], v[182:185], v[136:139], v[66:81]
	ds_read_b128 v[182:185], v207 offset:29248
	ds_read_b128 v[202:205], v207 offset:29280
	s_waitcnt lgkmcnt(1)
	v_mfma_f32_32x32x16_bf16 v[50:65], v[182:185], v[136:139], v[50:65]
	v_mfma_f32_32x32x16_bf16 v[66:81], v[198:201], v[132:135], v[66:81]
	ds_read_b128 v[182:185], v207 offset:22656
	ds_read_b128 v[198:201], v207 offset:22688
	global_load_dwordx4 v[94:97], v[94:95], off offset:128
	s_waitcnt lgkmcnt(1)
	v_mfma_f32_32x32x16_bf16 v[66:81], v[182:185], v[128:131], v[66:81]
	ds_read_b128 v[182:185], v207 offset:29312
	v_mfma_f32_32x32x16_bf16 v[50:65], v[202:205], v[132:135], v[50:65]
	ds_read2_b64 v[202:205], v211 offset0:192 offset1:194
	s_waitcnt lgkmcnt(2)
	v_mfma_f32_32x32x16_bf16 v[66:81], v[198:201], v[124:127], v[66:81]
	ds_read_b128 v[198:201], v207 offset:29344
	ds_read2_b64 v[206:209], v210 offset0:132 offset1:134
	s_waitcnt lgkmcnt(3)
	v_mfma_f32_32x32x16_bf16 v[50:65], v[182:185], v[128:131], v[50:65]
	ds_read2_b64 v[182:185], v210 offset0:128 offset1:130
	s_nop 6
	v_exp_f32_e32 v66, v66
	v_exp_f32_e32 v67, v67
	v_exp_f32_e32 v68, v68
	v_exp_f32_e32 v69, v69
	v_exp_f32_e32 v70, v70
	v_exp_f32_e32 v71, v71
	v_exp_f32_e32 v72, v72
	v_exp_f32_e32 v73, v73
	s_waitcnt lgkmcnt(2)
	v_mfma_f32_32x32x16_bf16 v[50:65], v[198:201], v[124:127], v[50:65]
	v_cvt_pk_bf16_f32 v198, v66, v67
	v_cvt_pk_bf16_f32 v199, v68, v69
	v_cvt_pk_bf16_f32 v200, v70, v71
	v_cvt_pk_bf16_f32 v201, v72, v73
	v_exp_f32_e32 v76, v76
	v_exp_f32_e32 v77, v77
	s_nop 5
	v_exp_f32_e32 v52, v52
	v_mfma_f32_32x32x16_bf16 v[34:49], v[202:205], v[198:201], v[34:49]
	ds_read2_b64 v[202:205], v211 offset0:196 offset1:198
	v_exp_f32_e32 v53, v53
	s_waitcnt lgkmcnt(1)
	v_mfma_f32_32x32x16_bf16 v[18:33], v[182:185], v[198:201], v[18:33]
	v_exp_f32_e32 v182, v74
	v_exp_f32_e32 v183, v75
	v_exp_f32_e32 v74, v78
	v_exp_f32_e32 v75, v79
	v_exp_f32_e32 v78, v80
	v_exp_f32_e32 v79, v81
	v_cvt_pk_bf16_f32 v198, v182, v183
	v_cvt_pk_bf16_f32 v199, v76, v77
	v_cvt_pk_bf16_f32 v200, v74, v75
	v_cvt_pk_bf16_f32 v201, v78, v79
	v_exp_f32_e32 v80, v50
	v_exp_f32_e32 v81, v51
	v_mfma_f32_32x32x16_bf16 v[18:33], v[206:209], v[198:201], v[18:33]
	ds_read2_b64 v[206:209], v210 offset0:136 offset1:138
	v_exp_f32_e32 v50, v54
	v_exp_f32_e32 v51, v55
	v_exp_f32_e32 v54, v56
	v_exp_f32_e32 v55, v57
	v_exp_f32_e32 v184, v58
	v_exp_f32_e32 v185, v59
	s_waitcnt lgkmcnt(1)
	v_mfma_f32_32x32x16_bf16 v[34:49], v[202:205], v[198:201], v[34:49]
	ds_read2_b64 v[202:205], v211 offset0:200 offset1:202
	v_cvt_pk_bf16_f32 v198, v80, v81
	v_cvt_pk_bf16_f32 v199, v52, v53
	v_cvt_pk_bf16_f32 v200, v50, v51
	v_cvt_pk_bf16_f32 v201, v54, v55
	v_exp_f32_e32 v58, v60
	v_exp_f32_e32 v59, v61
	s_waitcnt lgkmcnt(1)
	v_mfma_f32_32x32x16_bf16 v[18:33], v[206:209], v[198:201], v[18:33]
	ds_read2_b64 v[206:209], v210 offset0:140 offset1:142
	v_exp_f32_e32 v56, v62
	v_exp_f32_e32 v57, v63
	v_exp_f32_e32 v60, v64
	v_exp_f32_e32 v61, v65
	v_add_u32_e32 v63, s15, v188
	v_add_u32_e32 v62, s15, v189
	s_waitcnt lgkmcnt(1)
	v_mfma_f32_32x32x16_bf16 v[34:49], v[202:205], v[198:201], v[34:49]
	ds_read2_b64 v[202:205], v211 offset0:204 offset1:206
	v_cvt_pk_bf16_f32 v198, v184, v185
	v_cvt_pk_bf16_f32 v199, v58, v59
	v_cvt_pk_bf16_f32 v200, v56, v57
	v_cvt_pk_bf16_f32 v201, v60, v61
	s_waitcnt vmcnt(3)
	ds_write_b128 v63, v[90:93]
	s_waitcnt lgkmcnt(2)
	v_mfma_f32_32x32x16_bf16 v[18:33], v[206:209], v[198:201], v[18:33]
	s_waitcnt lgkmcnt(1)
	v_mfma_f32_32x32x16_bf16 v[34:49], v[202:205], v[198:201], v[34:49]
	s_and_saveexec_b64 s[16:17], s[0:1]
	s_xor_b64 s[16:17], exec, s[16:17]
	s_cbranch_execz .LBB0_556
	s_waitcnt vmcnt(2)
	ds_write_b128 v62, v[82:85] offset:13312
	s_waitcnt vmcnt(1)
	ds_write_b128 v63, v[86:89] offset:22528
